# sc1 write-through also on the 16 fragment (kbF/vbF) dwordx4 stores per item in P3, on top of P1 and P10
# baseline (speedup 1.0000x reference)
.LBB0_325:
	s_or_b64 exec, exec, s[16:17]
	s_waitcnt vmcnt(0)
	v_or_b32_e32 v35, s42, v22
	v_mov_b64_e32 v[70:71], s[20:21]
	s_mulk_i32 s43, 0x4e00
	v_mad_u64_u32 v[62:63], s[16:17], v35, s49, v[70:71]
	v_add_u32_e32 v63, s43, v63
	v_mov_b32_e32 v41, v7
	v_lshl_add_u64 v[62:63], v[62:63], 0, v[40:41]
	v_mov_b32_e32 v43, v7
	v_lshl_add_u64 v[62:63], v[62:63], 0, v[42:43]
	v_lshl_add_u64 v[62:63], v[62:63], 0, s[38:39]
	v_lshl_add_u64 v[64:65], v[62:63], 0, v[44:45]
	v_lshl_add_u64 v[66:67], v[62:63], 0, v[46:47]
	global_load_dwordx4 v[88:91], v[64:65], off
	global_load_dwordx4 v[92:95], v[66:67], off
	v_lshl_add_u64 v[64:65], v[62:63], 0, v[48:49]
	v_lshl_add_u64 v[66:67], v[62:63], 0, v[50:51]
	global_load_dwordx4 v[96:99], v[64:65], off
	global_load_dwordx4 v[100:103], v[66:67], off
	v_lshl_add_u64 v[64:65], v[62:63], 0, v[52:53]
	v_lshl_add_u64 v[66:67], v[62:63], 0, v[54:55]
	global_load_dwordx4 v[104:107], v[64:65], off
	global_load_dwordx4 v[108:111], v[66:67], off
	v_lshl_add_u64 v[64:65], v[62:63], 0, v[56:57]
	v_lshl_add_u64 v[62:63], v[62:63], 0, v[58:59]
	global_load_dwordx4 v[112:115], v[64:65], off
	global_load_dwordx4 v[116:119], v[62:63], off
	s_lshl_b32 s16, s54, 3
	v_add_u32_e32 v78, s16, v1
	v_add_u32_e32 v76, s16, v23
	v_add_u32_e32 v74, s16, v25
	v_add_u32_e32 v72, s16, v29
	v_add_u32_e32 v68, s16, v31
	v_add_u32_e32 v66, s16, v80
	v_add_u32_e32 v64, s16, v81
	v_ashrrev_i32_e32 v79, 31, v78
	v_add_u32_e32 v62, s16, v82
	v_ashrrev_i32_e32 v77, 31, v76
	v_ashrrev_i32_e32 v75, 31, v74
	v_ashrrev_i32_e32 v73, 31, v72
	v_ashrrev_i32_e32 v69, 31, v68
	v_ashrrev_i32_e32 v67, 31, v66
	v_ashrrev_i32_e32 v65, 31, v64
	v_lshlrev_b64 v[120:121], 11, v[78:79]
	s_lshl_b32 s17, s75, 3
	v_ashrrev_i32_e32 v63, 31, v62
	v_lshlrev_b64 v[122:123], 11, v[76:77]
	v_lshlrev_b64 v[124:125], 11, v[74:75]
	v_lshlrev_b64 v[126:127], 11, v[72:73]
	v_lshlrev_b64 v[128:129], 11, v[68:69]
	v_lshlrev_b64 v[130:131], 11, v[66:67]
	v_lshlrev_b64 v[132:133], 11, v[64:65]
	v_or_b32_e32 v35, v120, v24
	v_lshlrev_b64 v[134:135], 11, v[62:63]
	v_or_b32_e32 v37, v122, v24
	v_or_b32_e32 v39, v124, v24
	v_or_b32_e32 v41, v126, v24
	v_or_b32_e32 v43, v128, v24
	v_or_b32_e32 v61, v130, v24
	v_or_b32_e32 v132, v132, v24
	v_or_b32_e32 v120, s17, v35
	v_or_b32_e32 v122, s17, v37
	v_or_b32_e32 v124, s17, v39
	v_or_b32_e32 v126, s17, v41
	v_or_b32_e32 v128, s17, v43
	v_or_b32_e32 v130, s17, v61
	v_or_b32_e32 v132, s17, v132
	v_lshlrev_b64 v[120:121], 10, v[120:121]
	v_or_b32_e32 v35, v134, v24
	v_lshlrev_b64 v[122:123], 10, v[122:123]
	v_lshlrev_b64 v[124:125], 10, v[124:125]
	v_lshlrev_b64 v[126:127], 10, v[126:127]
	v_lshlrev_b64 v[128:129], 10, v[128:129]
	v_lshlrev_b64 v[130:131], 10, v[130:131]
	v_lshlrev_b64 v[132:133], 10, v[132:133]
	v_lshl_add_u64 v[120:121], v[26:27], 0, v[120:121]
	v_or_b32_e32 v134, s17, v35
	v_or_b32_e32 v35, s42, v28
	v_lshl_add_u64 v[122:123], v[26:27], 0, v[122:123]
	v_lshl_add_u64 v[124:125], v[26:27], 0, v[124:125]
	v_lshl_add_u64 v[126:127], v[26:27], 0, v[126:127]
	v_lshl_add_u64 v[128:129], v[26:27], 0, v[128:129]
	v_lshl_add_u64 v[130:131], v[26:27], 0, v[130:131]
	v_lshl_add_u64 v[132:133], v[26:27], 0, v[132:133]
	v_mad_u64_u32 v[70:71], s[16:17], v35, s49, v[70:71]
	v_add_u32_e32 v71, s43, v71
	v_mov_b32_e32 v61, v7
	v_lshl_add_u64 v[70:71], v[70:71], 0, v[60:61]
	v_lshlrev_b64 v[78:79], 10, v[78:79]
	s_lshl_b32 s16, s75, 2
	v_lshlrev_b64 v[76:77], 10, v[76:77]
	s_waitcnt vmcnt(7)
	global_store_dwordx4 v[120:121], v[88:91], off sc1
	s_waitcnt vmcnt(7)
	global_store_dwordx4 v[122:123], v[92:95], off sc1
	s_waitcnt vmcnt(7)
	global_store_dwordx4 v[124:125], v[96:99], off sc1
	s_waitcnt vmcnt(7)
	global_store_dwordx4 v[126:127], v[100:103], off sc1
	s_waitcnt vmcnt(7)
	global_store_dwordx4 v[128:129], v[104:107], off sc1
	s_waitcnt vmcnt(7)
	global_store_dwordx4 v[130:131], v[108:111], off sc1
	s_waitcnt vmcnt(7)
	global_store_dwordx4 v[132:133], v[112:115], off sc1
	v_lshlrev_b64 v[88:89], 10, v[134:135]
	v_lshl_add_u64 v[88:89], v[26:27], 0, v[88:89]
	v_lshlrev_b64 v[74:75], 10, v[74:75]
	s_waitcnt vmcnt(7)
	global_store_dwordx4 v[88:89], v[116:119], off sc1
	v_lshlrev_b32_e32 v88, 1, v22
	v_mov_b32_e32 v89, v7
	v_lshl_add_u64 v[70:71], v[70:71], 0, v[88:89]
	v_lshl_add_u64 v[70:71], v[70:71], 0, s[40:41]
	v_lshl_add_u64 v[88:89], v[70:71], 0, v[44:45]
	v_add_co_u32_e32 v90, vcc, s67, v88
	v_lshlrev_b64 v[72:73], 10, v[72:73]
	s_nop 0
	v_addc_co_u32_e32 v91, vcc, 0, v89, vcc
	v_add_co_u32_e32 v92, vcc, s68, v88
	v_lshlrev_b64 v[68:69], 10, v[68:69]
	s_nop 0
	v_addc_co_u32_e32 v93, vcc, 0, v89, vcc
	v_add_co_u32_e32 v94, vcc, s69, v88
	v_lshlrev_b64 v[66:67], 10, v[66:67]
	s_nop 0
	v_addc_co_u32_e32 v95, vcc, 0, v89, vcc
	v_add_co_u32_e32 v96, vcc, s70, v88
	v_lshlrev_b64 v[64:65], 10, v[64:65]
	s_nop 0
	v_addc_co_u32_e32 v97, vcc, 0, v89, vcc
	v_add_co_u32_e32 v98, vcc, s71, v88
	v_lshlrev_b64 v[62:63], 10, v[62:63]
	s_nop 0
	v_addc_co_u32_e32 v99, vcc, 0, v89, vcc
	v_add_co_u32_e32 v100, vcc, s72, v88
	s_add_i32 s74, s74, s48
	s_nop 0
	v_addc_co_u32_e32 v101, vcc, 0, v89, vcc
	v_add_co_u32_e32 v102, vcc, s73, v88
	s_cmpk_lt_i32 s74, 0x400
	s_nop 0
	v_addc_co_u32_e32 v103, vcc, 0, v89, vcc
	global_load_ushort v35, v[88:89], off
	global_load_ushort v37, v[90:91], off offset:3584
	global_load_ushort v39, v[92:93], off offset:3072
	global_load_ushort v41, v[94:95], off offset:2560
	global_load_ushort v43, v[96:97], off
	global_load_ushort v61, v[98:99], off offset:3584
	global_load_ushort v104, v[100:101], off offset:3072
	global_load_ushort v105, v[102:103], off offset:2560
	v_lshl_add_u64 v[88:89], v[70:71], 0, v[46:47]
	v_add_co_u32_e32 v90, vcc, s67, v88
	s_nop 1
	v_addc_co_u32_e32 v91, vcc, 0, v89, vcc
	v_add_co_u32_e32 v92, vcc, s68, v88
	s_nop 1
	v_addc_co_u32_e32 v93, vcc, 0, v89, vcc
	v_add_co_u32_e32 v94, vcc, s69, v88
	s_nop 1
	v_addc_co_u32_e32 v95, vcc, 0, v89, vcc
	v_add_co_u32_e32 v96, vcc, s70, v88
	s_nop 1
	v_addc_co_u32_e32 v97, vcc, 0, v89, vcc
	v_add_co_u32_e32 v98, vcc, s71, v88
	s_nop 1
	v_addc_co_u32_e32 v99, vcc, 0, v89, vcc
	v_add_co_u32_e32 v100, vcc, s72, v88
	s_nop 1
	v_addc_co_u32_e32 v101, vcc, 0, v89, vcc
	v_add_co_u32_e32 v102, vcc, s73, v88
	s_nop 1
	v_addc_co_u32_e32 v103, vcc, 0, v89, vcc
	global_load_ushort v106, v[88:89], off
	global_load_ushort v107, v[90:91], off offset:3584
	global_load_ushort v108, v[92:93], off offset:3072
	global_load_ushort v109, v[94:95], off offset:2560
	global_load_ushort v110, v[96:97], off
	global_load_ushort v111, v[98:99], off offset:3584
	global_load_ushort v112, v[100:101], off offset:3072
	global_load_ushort v113, v[102:103], off offset:2560
	v_lshl_add_u64 v[88:89], v[70:71], 0, v[48:49]
	v_add_co_u32_e32 v90, vcc, s67, v88
	s_nop 1
	v_addc_co_u32_e32 v91, vcc, 0, v89, vcc
	v_add_co_u32_e32 v92, vcc, s68, v88
	s_nop 1
	v_addc_co_u32_e32 v93, vcc, 0, v89, vcc
	v_add_co_u32_e32 v94, vcc, s69, v88
	s_nop 1
	v_addc_co_u32_e32 v95, vcc, 0, v89, vcc
	v_add_co_u32_e32 v96, vcc, s70, v88
	s_nop 1
	v_addc_co_u32_e32 v97, vcc, 0, v89, vcc
	v_add_co_u32_e32 v98, vcc, s71, v88
	s_nop 1
	v_addc_co_u32_e32 v99, vcc, 0, v89, vcc
	v_add_co_u32_e32 v100, vcc, s72, v88
	s_nop 1
	v_addc_co_u32_e32 v101, vcc, 0, v89, vcc
	v_add_co_u32_e32 v102, vcc, s73, v88
	s_nop 1
	v_addc_co_u32_e32 v103, vcc, 0, v89, vcc
	global_load_ushort v114, v[88:89], off
	global_load_ushort v115, v[90:91], off offset:3584
	global_load_ushort v116, v[92:93], off offset:3072
	global_load_ushort v117, v[94:95], off offset:2560
	global_load_ushort v118, v[96:97], off
	global_load_ushort v119, v[98:99], off offset:3584
	global_load_ushort v120, v[100:101], off offset:3072
	global_load_ushort v121, v[102:103], off offset:2560
	v_lshl_add_u64 v[88:89], v[70:71], 0, v[50:51]
	v_add_co_u32_e32 v90, vcc, s67, v88
	s_nop 1
	v_addc_co_u32_e32 v91, vcc, 0, v89, vcc
	v_add_co_u32_e32 v92, vcc, s68, v88
	s_nop 1
	v_addc_co_u32_e32 v93, vcc, 0, v89, vcc
	v_add_co_u32_e32 v94, vcc, s69, v88
	s_nop 1
	v_addc_co_u32_e32 v95, vcc, 0, v89, vcc
	v_add_co_u32_e32 v96, vcc, s70, v88
	s_nop 1
	v_addc_co_u32_e32 v97, vcc, 0, v89, vcc
	v_add_co_u32_e32 v98, vcc, s71, v88
	s_nop 1
	v_addc_co_u32_e32 v99, vcc, 0, v89, vcc
	v_add_co_u32_e32 v100, vcc, s72, v88
	s_nop 1
	v_addc_co_u32_e32 v101, vcc, 0, v89, vcc
	v_add_co_u32_e32 v102, vcc, s73, v88
	s_nop 1
	v_addc_co_u32_e32 v103, vcc, 0, v89, vcc
	global_load_ushort v122, v[88:89], off
	global_load_ushort v123, v[90:91], off offset:3584
	global_load_ushort v124, v[92:93], off offset:3072
	global_load_ushort v125, v[94:95], off offset:2560
	global_load_ushort v126, v[96:97], off
	global_load_ushort v127, v[98:99], off offset:3584
	global_load_ushort v128, v[100:101], off offset:3072
	s_nop 0
	global_load_ushort v103, v[102:103], off offset:2560
	s_waitcnt vmcnt(30)
	v_lshl_or_b32 v88, v37, 16, v35
	v_or_b32_e32 v35, v78, v30
	v_or_b32_e32 v78, s16, v35
	v_or_b32_e32 v35, v76, v30
	v_or_b32_e32 v76, s16, v35
	v_or_b32_e32 v35, v74, v30
	v_or_b32_e32 v74, s16, v35
	v_or_b32_e32 v35, v72, v30
	v_or_b32_e32 v72, s16, v35
	v_lshlrev_b64 v[78:79], 11, v[78:79]
	v_lshlrev_b64 v[76:77], 11, v[76:77]
	v_lshlrev_b64 v[74:75], 11, v[74:75]
	v_lshlrev_b64 v[72:73], 11, v[72:73]
	v_or_b32_e32 v78, v78, v87
	v_or_b32_e32 v76, v76, v87
	v_or_b32_e32 v74, v74, v87
	v_or_b32_e32 v72, v72, v87
	s_waitcnt vmcnt(28)
	v_lshl_or_b32 v89, v41, 16, v39
	s_waitcnt vmcnt(26)
	v_lshl_or_b32 v90, v61, 16, v43
	s_waitcnt vmcnt(24)
	v_lshl_or_b32 v91, v105, 16, v104
	s_waitcnt vmcnt(22)
	v_lshl_or_b32 v92, v107, 16, v106
	s_waitcnt vmcnt(20)
	v_lshl_or_b32 v93, v109, 16, v108
	s_waitcnt vmcnt(18)
	v_lshl_or_b32 v94, v111, 16, v110
	s_waitcnt vmcnt(16)
	v_lshl_or_b32 v95, v113, 16, v112
	v_lshl_add_u64 v[78:79], s[22:23], 0, v[78:79]
	v_lshl_add_u64 v[76:77], s[22:23], 0, v[76:77]
	v_lshl_add_u64 v[74:75], s[22:23], 0, v[74:75]
	v_lshl_add_u64 v[72:73], s[22:23], 0, v[72:73]
	global_store_dwordx4 v[78:79], v[88:91], off sc1
	global_store_dwordx4 v[76:77], v[92:95], off sc1
	s_waitcnt vmcnt(16)
	v_lshl_or_b32 v96, v115, 16, v114
	s_waitcnt vmcnt(14)
	v_lshl_or_b32 v97, v117, 16, v116
	s_waitcnt vmcnt(12)
	v_lshl_or_b32 v98, v119, 16, v118
	s_waitcnt vmcnt(10)
	v_lshl_or_b32 v99, v121, 16, v120
	global_store_dwordx4 v[74:75], v[96:99], off sc1
	s_waitcnt vmcnt(9)
	v_lshl_or_b32 v100, v123, 16, v122
	s_waitcnt vmcnt(7)
	v_lshl_or_b32 v101, v125, 16, v124
	s_waitcnt vmcnt(5)
	v_lshl_or_b32 v102, v127, 16, v126
	s_waitcnt vmcnt(3)
	v_lshl_or_b32 v103, v103, 16, v128
	global_store_dwordx4 v[72:73], v[100:103], off sc1
	v_lshl_add_u64 v[72:73], v[70:71], 0, v[52:53]
	v_add_co_u32_e32 v74, vcc, s67, v72
	s_nop 1
	v_addc_co_u32_e32 v75, vcc, 0, v73, vcc
	v_add_co_u32_e32 v76, vcc, s68, v72
	s_nop 1
	v_addc_co_u32_e32 v77, vcc, 0, v73, vcc
	v_add_co_u32_e32 v78, vcc, s69, v72
	s_nop 1
	v_addc_co_u32_e32 v79, vcc, 0, v73, vcc
	v_add_co_u32_e32 v88, vcc, s70, v72
	s_nop 1
	v_addc_co_u32_e32 v89, vcc, 0, v73, vcc
	v_add_co_u32_e32 v90, vcc, s71, v72
	s_nop 1
	v_addc_co_u32_e32 v91, vcc, 0, v73, vcc
	v_add_co_u32_e32 v92, vcc, s72, v72
	s_nop 1
	v_addc_co_u32_e32 v93, vcc, 0, v73, vcc
	v_add_co_u32_e32 v94, vcc, s73, v72
	s_nop 1
	v_addc_co_u32_e32 v95, vcc, 0, v73, vcc
	global_load_ushort v35, v[72:73], off
	global_load_ushort v37, v[74:75], off offset:3584
	global_load_ushort v39, v[76:77], off offset:3072
	global_load_ushort v41, v[78:79], off offset:2560
	global_load_ushort v43, v[88:89], off
	global_load_ushort v61, v[90:91], off offset:3584
	global_load_ushort v96, v[92:93], off offset:3072
	global_load_ushort v97, v[94:95], off offset:2560
	v_lshl_add_u64 v[72:73], v[70:71], 0, v[54:55]
	v_add_co_u32_e32 v74, vcc, s67, v72
	s_nop 1
	v_addc_co_u32_e32 v75, vcc, 0, v73, vcc
	v_add_co_u32_e32 v76, vcc, s68, v72
	s_nop 1
	v_addc_co_u32_e32 v77, vcc, 0, v73, vcc
	v_add_co_u32_e32 v78, vcc, s69, v72
	s_nop 1
	v_addc_co_u32_e32 v79, vcc, 0, v73, vcc
	v_add_co_u32_e32 v88, vcc, s70, v72
	s_nop 1
	v_addc_co_u32_e32 v89, vcc, 0, v73, vcc
	v_add_co_u32_e32 v90, vcc, s71, v72
	s_nop 1
	v_addc_co_u32_e32 v91, vcc, 0, v73, vcc
	v_add_co_u32_e32 v92, vcc, s72, v72
	s_nop 1
	v_addc_co_u32_e32 v93, vcc, 0, v73, vcc
	v_add_co_u32_e32 v94, vcc, s73, v72
	s_nop 1
	v_addc_co_u32_e32 v95, vcc, 0, v73, vcc
	global_load_ushort v98, v[72:73], off
	global_load_ushort v99, v[74:75], off offset:3584
	global_load_ushort v100, v[76:77], off offset:3072
	global_load_ushort v101, v[78:79], off offset:2560
	global_load_ushort v102, v[88:89], off
	global_load_ushort v103, v[90:91], off offset:3584
	global_load_ushort v104, v[92:93], off offset:3072
	global_load_ushort v105, v[94:95], off offset:2560
	v_lshl_add_u64 v[72:73], v[70:71], 0, v[56:57]
	v_add_co_u32_e32 v74, vcc, s67, v72
	v_lshl_add_u64 v[70:71], v[70:71], 0, v[58:59]
	s_nop 0
	v_addc_co_u32_e32 v75, vcc, 0, v73, vcc
	v_add_co_u32_e32 v76, vcc, s68, v72
	s_nop 1
	v_addc_co_u32_e32 v77, vcc, 0, v73, vcc
	v_add_co_u32_e32 v78, vcc, s69, v72
	s_nop 1
	v_addc_co_u32_e32 v79, vcc, 0, v73, vcc
	v_add_co_u32_e32 v88, vcc, s70, v72
	s_nop 1
	v_addc_co_u32_e32 v89, vcc, 0, v73, vcc
	v_add_co_u32_e32 v90, vcc, s71, v72
	s_nop 1
	v_addc_co_u32_e32 v91, vcc, 0, v73, vcc
	v_add_co_u32_e32 v92, vcc, s72, v72
	s_nop 1
	v_addc_co_u32_e32 v93, vcc, 0, v73, vcc
	v_add_co_u32_e32 v94, vcc, s73, v72
	s_nop 1
	v_addc_co_u32_e32 v95, vcc, 0, v73, vcc
	global_load_ushort v106, v[72:73], off
	global_load_ushort v107, v[74:75], off offset:3584
	global_load_ushort v108, v[76:77], off offset:3072
	global_load_ushort v109, v[78:79], off offset:2560
	global_load_ushort v110, v[88:89], off
	global_load_ushort v111, v[90:91], off offset:3584
	global_load_ushort v112, v[92:93], off offset:3072
	s_nop 0
	global_load_ushort v94, v[94:95], off offset:2560
	v_add_co_u32_e32 v72, vcc, s67, v70
	s_nop 1
	v_addc_co_u32_e32 v73, vcc, 0, v71, vcc
	v_add_co_u32_e32 v74, vcc, s68, v70
	s_nop 1
	v_addc_co_u32_e32 v75, vcc, 0, v71, vcc
	v_add_co_u32_e32 v76, vcc, s69, v70
	s_nop 1
	v_addc_co_u32_e32 v77, vcc, 0, v71, vcc
	v_add_co_u32_e32 v78, vcc, s70, v70
	s_nop 1
	v_addc_co_u32_e32 v79, vcc, 0, v71, vcc
	v_add_co_u32_e32 v88, vcc, s71, v70
	s_nop 1
	v_addc_co_u32_e32 v89, vcc, 0, v71, vcc
	v_add_co_u32_e32 v90, vcc, s72, v70
	s_nop 1
	v_addc_co_u32_e32 v91, vcc, 0, v71, vcc
	v_add_co_u32_e32 v92, vcc, s73, v70
	s_nop 1
	v_addc_co_u32_e32 v93, vcc, 0, v71, vcc
	global_load_ushort v95, v[70:71], off
	global_load_ushort v113, v[72:73], off offset:3584
	global_load_ushort v114, v[74:75], off offset:3072
	global_load_ushort v115, v[76:77], off offset:2560
	s_nop 0
	global_load_ushort v78, v[78:79], off
	s_nop 0
	global_load_ushort v79, v[88:89], off offset:3584
	global_load_ushort v116, v[90:91], off offset:3072
	global_load_ushort v117, v[92:93], off offset:2560
	s_waitcnt vmcnt(30)
	v_lshl_or_b32 v70, v37, 16, v35
	v_or_b32_e32 v35, v68, v30
	v_or_b32_e32 v68, s16, v35
	v_or_b32_e32 v35, v66, v30
	v_or_b32_e32 v66, s16, v35
	v_or_b32_e32 v35, v64, v30
	v_or_b32_e32 v64, s16, v35
	v_or_b32_e32 v35, v62, v30
	v_or_b32_e32 v62, s16, v35
	v_lshlrev_b64 v[68:69], 11, v[68:69]
	v_lshlrev_b64 v[66:67], 11, v[66:67]
	v_lshlrev_b64 v[64:65], 11, v[64:65]
	v_lshlrev_b64 v[62:63], 11, v[62:63]
	v_or_b32_e32 v68, v68, v87
	v_or_b32_e32 v66, v66, v87
	v_or_b32_e32 v64, v64, v87
	v_or_b32_e32 v62, v62, v87
	s_waitcnt vmcnt(28)
	v_lshl_or_b32 v71, v41, 16, v39
	s_waitcnt vmcnt(26)
	v_lshl_or_b32 v72, v61, 16, v43
	s_waitcnt vmcnt(24)
	v_lshl_or_b32 v73, v97, 16, v96
	s_waitcnt vmcnt(22)
	v_lshl_or_b32 v74, v99, 16, v98
	s_waitcnt vmcnt(20)
	v_lshl_or_b32 v75, v101, 16, v100
	s_waitcnt vmcnt(18)
	v_lshl_or_b32 v76, v103, 16, v102
	s_waitcnt vmcnt(16)
	v_lshl_or_b32 v77, v105, 16, v104
	v_lshl_add_u64 v[68:69], s[22:23], 0, v[68:69]
	v_lshl_add_u64 v[66:67], s[22:23], 0, v[66:67]
	v_lshl_add_u64 v[64:65], s[22:23], 0, v[64:65]
	v_lshl_add_u64 v[62:63], s[22:23], 0, v[62:63]
	global_store_dwordx4 v[68:69], v[70:73], off sc1
	global_store_dwordx4 v[66:67], v[74:77], off sc1
	s_waitcnt vmcnt(16)
	v_lshl_or_b32 v88, v107, 16, v106
	s_waitcnt vmcnt(14)
	v_lshl_or_b32 v89, v109, 16, v108
	s_waitcnt vmcnt(12)
	v_lshl_or_b32 v90, v111, 16, v110
	s_waitcnt vmcnt(10)
	v_lshl_or_b32 v91, v94, 16, v112
	global_store_dwordx4 v[64:65], v[88:91], off sc1
	s_waitcnt vmcnt(9)
	v_lshl_or_b32 v92, v113, 16, v95
	s_waitcnt vmcnt(7)
	v_lshl_or_b32 v93, v115, 16, v114
	s_waitcnt vmcnt(5)
	v_lshl_or_b32 v94, v79, 16, v78
	s_waitcnt vmcnt(3)
	v_lshl_or_b32 v95, v117, 16, v116
	global_store_dwordx4 v[62:63], v[92:95], off sc1
	s_cbranch_scc0 .LBB0_360
